# speedup vs baseline: 1.0008x; 1.0008x over previous
_Z6k_gramILi0EEvPK15HIP_vector_typeIjLj4EEPyPf:
	s_mov_b32 s78, 0
	s_load_dwordx4 s[8:11], s[0:1], 0x0
	s_load_dwordx2 s[4:5], s[0:1], 0x10
	s_lshl_b32 s0, s2, 2
	s_and_b32 s0, s0, 28
	s_ashr_i32 s1, s2, 6
	s_add_i32 s16, s0, s1
	v_readfirstlane_b32 s23, v0
	s_ashr_i32 s17, s16, 31
	s_lshr_b32 s21, s23, 6
	s_bfe_u32 s18, s23, 0x20006
	s_lshr_b32 s22, s2, 3
	s_bfe_u32 s20, s2, 0x30003
	s_lshl_b64 s[0:1], s[16:17], 20
	s_waitcnt lgkmcnt(0)
	s_add_u32 s12, s8, s0
	v_mov_b32_e32 v1, 0x20000
	s_addc_u32 s0, s9, s1
	s_lshl_b32 s1, s20, 2
	v_lshl_or_b32 v1, v0, 2, v1
	v_bfrev_b32_e32 v2, 1
	s_cmp_lt_u32 s20, 4
	ds_write_b32 v1, v2
	s_mov_b32 s24, 4
	s_mov_b32 s15, 0x20000
	s_and_b32 s13, s0, 0xffff
	s_mov_b32 s14, 0x100000
	v_lshlrev_b32_e32 v166, 4, v0
	s_lshl_b32 s25, s21, 10
	s_lshl_b32 s0, s20, 17
	s_mov_b32 m0, s25
	s_nop 0
	buffer_load_dwordx4 v166, s[12:15], s0 offen lds
	s_add_i32 s26, s25, 0x2000
	s_or_b32 s2, s0, 0x2000
	s_mov_b32 m0, s26
	s_nop 0
	buffer_load_dwordx4 v166, s[12:15], s2 offen lds
	s_add_i32 s27, s25, 0x4000
	s_or_b32 s2, s0, 0x8000
	s_mov_b32 m0, s27
	s_nop 0
	buffer_load_dwordx4 v166, s[12:15], s2 offen lds
	s_add_i32 s28, s25, 0x6000
	s_or_b32 s2, s0, 0xa000
	s_mov_b32 m0, s28
	s_nop 0
	buffer_load_dwordx4 v166, s[12:15], s2 offen lds
	s_add_i32 s34, s25, 0x10000
	s_or_b32 s2, s0, 0x10000
	s_mov_b32 m0, s34
	s_nop 0
	buffer_load_dwordx4 v166, s[12:15], s2 offen lds
	s_add_i32 s35, s25, 0x12000
	s_or_b32 s2, s0, 0x12000
	s_mov_b32 m0, s35
	s_nop 0
	buffer_load_dwordx4 v166, s[12:15], s2 offen lds
	s_add_i32 s36, s25, 0x14000
	s_or_b32 s2, s0, 0x18000
	s_mov_b32 m0, s36
	s_nop 0
	buffer_load_dwordx4 v166, s[12:15], s2 offen lds
	s_add_i32 s37, s25, 0x16000
	s_or_b32 s2, s0, 0x1a000
	s_mov_b32 m0, s37
	s_nop 0
	buffer_load_dwordx4 v166, s[12:15], s2 offen lds
	s_add_i32 s29, s25, 0x8000
	s_or_b32 s2, s0, 0x4000
	s_mov_b32 m0, s29
	s_nop 0
	buffer_load_dwordx4 v166, s[12:15], s2 offen lds
	s_add_i32 s30, s25, 0xa000
	s_or_b32 s2, s0, 0x6000
	s_mov_b32 m0, s30
	s_nop 0
	buffer_load_dwordx4 v166, s[12:15], s2 offen lds
	s_add_i32 s31, s25, 0xc000
	s_or_b32 s2, s0, 0xc000
	s_mov_b32 m0, s31
	s_nop 0
	buffer_load_dwordx4 v166, s[12:15], s2 offen lds
	s_add_i32 s33, s25, 0xe000
	s_or_b32 s2, s0, 0xe000
	s_mov_b32 m0, s33
	s_nop 0
	buffer_load_dwordx4 v166, s[12:15], s2 offen lds
	s_add_i32 s38, s25, 0x18000
	s_or_b32 s2, s0, 0x14000
	s_mov_b32 m0, s38
	s_nop 0
	buffer_load_dwordx4 v166, s[12:15], s2 offen lds
	s_add_i32 s39, s25, 0x1a000
	s_or_b32 s2, s0, 0x16000
	s_mov_b32 m0, s39
	s_nop 0
	buffer_load_dwordx4 v166, s[12:15], s2 offen lds
	s_add_i32 s40, s25, 0x1c000
	s_or_b32 s2, s0, 0x1c000
	s_mov_b32 m0, s40
	s_nop 0
	buffer_load_dwordx4 v166, s[12:15], s2 offen lds
	s_add_i32 s42, s25, 0x1e000
	s_or_b32 s2, s0, 0x1e000
	s_mov_b32 m0, s42
	s_nop 0
	buffer_load_dwordx4 v166, s[12:15], s2 offen lds
	s_lshl_b32 s0, s23, 9
	s_lshl_b32 s2, s23, 8
	v_and_b32_e32 v167, 15, v0
	v_bfe_u32 v160, v0, 4, 2
	s_and_b32 s0, s0, 0x10000
	s_and_b32 s2, s2, 0x4000
	v_lshlrev_b32_e32 v128, 9, v160
	v_lshlrev_b32_e32 v129, 4, v167
	s_or_b32 s0, s0, s2
	v_or3_b32 v124, s0, v128, v129
	s_waitcnt vmcnt(8)
	s_waitcnt lgkmcnt(0)
	s_barrier
	ds_read_b128 v[0:3], v124
	ds_read_b128 v[4:7], v124 offset:256
	ds_read_b128 v[8:11], v124 offset:2048
	ds_read_b128 v[12:15], v124 offset:2304
	ds_read_b128 v[16:19], v124 offset:4096
	ds_read_b128 v[20:23], v124 offset:4352
	ds_read_b128 v[24:27], v124 offset:6144
	ds_read_b128 v[28:31], v124 offset:6400
	ds_read_b128 v[32:35], v124 offset:8192
	ds_read_b128 v[36:39], v124 offset:8448
	ds_read_b128 v[40:43], v124 offset:10240
	ds_read_b128 v[44:47], v124 offset:10496
	ds_read_b128 v[48:51], v124 offset:12288
	ds_read_b128 v[52:55], v124 offset:12544
	ds_read_b128 v[56:59], v124 offset:14336
	ds_read_b128 v[60:63], v124 offset:14592
	s_lshr_b32 s41, s23, 8
	s_lshl_b32 s0, s41, 14
	s_lshl_b32 s50, s24, 2
	v_or3_b32 v168, s0, v128, v129
	s_or_b32 s43, s18, s1
	s_lshl_b32 s0, s16, 10
	s_lshl_b32 s1, s43, 5
	ds_read_b128 v[128:131], v168
	ds_read_b128 v[132:135], v168 offset:256
	ds_read_b128 v[136:139], v168 offset:2048
	ds_read_b128 v[140:143], v168 offset:2304
	s_or_b32 s0, s1, s0
	v_or_b32_e32 v144, s0, v167
	v_lshlrev_b32_e32 v146, 2, v160
	v_ashrrev_i32_e32 v145, 31, v144
	v_lshl_add_u64 v[164:165], v[144:145], 2, s[4:5]
	v_or_b32_e32 v144, 1, v146
	v_cmp_eq_u32_e64 s[2:3], v144, v167
	v_or_b32_e32 v144, 2, v146
	s_waitcnt vmcnt(8)
	v_cmp_eq_u32_e64 s[4:5], v144, v167
	v_or_b32_e32 v144, 3, v146
	s_add_i32 s44, s50, 3
	s_lshl_b32 s45, s22, 2
	v_cmp_eq_u32_e64 s[0:1], v146, v167
	v_cmp_eq_u32_e64 s[6:7], v144, v167
	v_add_u32_e32 v169, 0x10000, v168
	v_add_u32_e32 v170, 0x10100, v168
	v_add_u32_e32 v171, 0x10800, v168
	v_add_u32_e32 v172, 0x10900, v168
	s_barrier
	s_add_i32 s8, s45, 28
	s_and_b32 s8, s8, 28
	s_add_i32 s8, s41, s8
	s_lshl_b32 s8, s8, 1
	s_add_i32 s9, s8, 4
	s_add_i32 s8, s8, 5
	v_mov_b32_e32 v148, s9
	v_mov_b32_e32 v149, s8
	ds_read_b128 v[148:151], v168 offset:4096
	s_waitcnt lgkmcnt(4)
	v_mfma_f32_16x16x32_bf16 v[144:147], v[0:3], v[128:131], 0
	v_mfma_f32_16x16x32_bf16 v[128:131], v[4:7], v[128:131], 0
	ds_read_b128 v[156:159], v168 offset:4352
	s_waitcnt lgkmcnt(4)
	v_mfma_f32_16x16x32_bf16 v[152:155], v[0:3], v[132:135], 0
	v_mfma_f32_16x16x32_bf16 v[132:135], v[4:7], v[132:135], 0
	s_waitcnt lgkmcnt(3)
	v_mfma_f32_16x16x32_bf16 v[144:147], v[8:11], v[136:139], v[144:147]
	ds_read_b128 v[174:177], v168 offset:6144
	v_mfma_f32_16x16x32_bf16 v[128:131], v[12:15], v[136:139], v[128:131]
	s_waitcnt lgkmcnt(3)
	v_mfma_f32_16x16x32_bf16 v[136:139], v[8:11], v[140:143], v[152:155]
	s_nop 2
	ds_read_b128 v[152:155], v168 offset:6400
	v_mfma_f32_16x16x32_bf16 v[132:135], v[12:15], v[140:143], v[132:135]
	s_waitcnt lgkmcnt(3)
	v_mfma_f32_16x16x32_bf16 v[140:143], v[16:19], v[148:151], v[144:147]
	s_nop 2
	ds_read_b128 v[144:147], v168 offset:8192
	v_mfma_f32_16x16x32_bf16 v[128:131], v[20:23], v[148:151], v[128:131]
	ds_read_b128 v[148:151], v168 offset:8448
	s_waitcnt lgkmcnt(4)
	v_mfma_f32_16x16x32_bf16 v[136:139], v[16:19], v[156:159], v[136:139]
	v_mfma_f32_16x16x32_bf16 v[132:135], v[20:23], v[156:159], v[132:135]
	ds_read_b128 v[156:159], v168 offset:10240
	s_waitcnt lgkmcnt(4)
	v_mfma_f32_16x16x32_bf16 v[140:143], v[24:27], v[174:177], v[140:143]
	v_mfma_f32_16x16x32_bf16 v[128:131], v[28:31], v[174:177], v[128:131]
	s_waitcnt lgkmcnt(3)
	v_mfma_f32_16x16x32_bf16 v[136:139], v[24:27], v[152:155], v[136:139]
	ds_read_b128 v[174:177], v168 offset:10496
	v_mfma_f32_16x16x32_bf16 v[132:135], v[28:31], v[152:155], v[132:135]
	ds_read_b128 v[152:155], v168 offset:12288
	s_waitcnt lgkmcnt(4)
	v_mfma_f32_16x16x32_bf16 v[140:143], v[32:35], v[144:147], v[140:143]
	v_mfma_f32_16x16x32_bf16 v[128:131], v[36:39], v[144:147], v[128:131]
	ds_read_b128 v[144:147], v168 offset:12544
	s_waitcnt lgkmcnt(4)
	v_mfma_f32_16x16x32_bf16 v[136:139], v[32:35], v[148:151], v[136:139]
	v_mfma_f32_16x16x32_bf16 v[132:135], v[36:39], v[148:151], v[132:135]
	ds_read_b128 v[148:151], v168 offset:14336
	s_waitcnt lgkmcnt(4)
	v_mfma_f32_16x16x32_bf16 v[140:143], v[40:43], v[156:159], v[140:143]
	v_mfma_f32_16x16x32_bf16 v[128:131], v[44:47], v[156:159], v[128:131]
	ds_read_b128 v[156:159], v168 offset:14592
	s_waitcnt lgkmcnt(4)
	v_mfma_f32_16x16x32_bf16 v[136:139], v[40:43], v[174:177], v[136:139]
	v_mfma_f32_16x16x32_bf16 v[132:135], v[44:47], v[174:177], v[132:135]
	s_waitcnt lgkmcnt(3)
	v_mfma_f32_16x16x32_bf16 v[140:143], v[48:51], v[152:155], v[140:143]
	ds_read_b128 v[174:177], v168 offset:32768
	v_mfma_f32_16x16x32_bf16 v[128:131], v[52:55], v[152:155], v[128:131]
	ds_read_b128 v[152:155], v168 offset:33024
	s_waitcnt lgkmcnt(4)
	v_mfma_f32_16x16x32_bf16 v[136:139], v[48:51], v[144:147], v[136:139]
	v_mfma_f32_16x16x32_bf16 v[132:135], v[52:55], v[144:147], v[132:135]
	ds_read_b128 v[144:147], v168 offset:34816
	s_waitcnt lgkmcnt(4)
	v_mfma_f32_16x16x32_bf16 v[140:143], v[56:59], v[148:151], v[140:143]
	v_mfma_f32_16x16x32_bf16 v[128:131], v[60:63], v[148:151], v[128:131]
	ds_read_b128 v[148:151], v168 offset:35072
	s_waitcnt lgkmcnt(4)
	v_mfma_f32_16x16x32_bf16 v[136:139], v[56:59], v[156:159], v[136:139]
	v_mfma_f32_16x16x32_bf16 v[132:135], v[60:63], v[156:159], v[132:135]
	s_waitcnt vmcnt(0)
	s_barrier
	ds_read_b128 v[64:67], v124 offset:32768
	ds_read_b128 v[68:71], v124 offset:33024
	ds_read_b128 v[72:75], v124 offset:34816
	ds_read_b128 v[76:79], v124 offset:35072
	ds_read_b128 v[80:83], v124 offset:36864
	ds_read_b128 v[84:87], v124 offset:37120
	ds_read_b128 v[88:91], v124 offset:38912
	ds_read_b128 v[92:95], v124 offset:39168
	ds_read_b128 v[96:99], v124 offset:40960
	ds_read_b128 v[100:103], v124 offset:41216
	ds_read_b128 v[104:107], v124 offset:43008
	ds_read_b128 v[108:111], v124 offset:43264
	ds_read_b128 v[112:115], v124 offset:45056
	ds_read_b128 v[116:119], v124 offset:45312
	ds_read_b128 v[120:123], v124 offset:47104
	ds_read_b128 v[124:127], v124 offset:47360
	ds_read_b128 v[174:177], v168 offset:32768
	ds_read_b128 v[152:155], v168 offset:33024
	ds_read_b128 v[144:147], v168 offset:34816
	ds_read_b128 v[148:151], v168 offset:35072
	s_waitcnt lgkmcnt(0)
	s_and_b32 s8, s45, 28
	s_add_i32 s8, s8, s41
	s_lshl_b32 s19, s8, 1
	s_or_b32 s51, s19, 1
	v_mov_b32_e32 v156, s51
	v_mov_b32_e32 v157, s19
	ds_read_b128 v[156:159], v168 offset:36864
	s_waitcnt lgkmcnt(4)
	v_mfma_f32_16x16x32_bf16 v[140:143], v[64:67], v[174:177], v[140:143]
	s_min_u32 s9, s44, 4
	s_add_i32 s46, s9, s45
	v_mov_b32_e32 v202, s19
	v_mfma_f32_16x16x32_bf16 v[128:131], v[68:71], v[174:177], v[128:131]
	v_mov_b32_e32 v206, s51
	s_and_b32 s46, s46, 28
	s_and_b32 s47, s9, 2
	s_lshl_b32 s9, s9, 14
	s_or_b32 s46, s47, s46
	s_and_b32 s9, s9, 0x4000
	ds_read_b128 v[174:177], v168 offset:37120
	s_waitcnt lgkmcnt(4)
	v_mfma_f32_16x16x32_bf16 v[136:139], v[64:67], v[152:155], v[136:139]
	s_lshl_b32 s46, s46, 15
	s_or_b32 s9, s46, s9
	s_mov_b32 m0, s25
	s_nop 0
	buffer_load_dwordx4 v166, s[12:15], s9 offen lds
	v_mfma_f32_16x16x32_bf16 v[132:135], v[68:71], v[152:155], v[132:135]
	ds_read_b128 v[152:155], v168 offset:38912
	s_waitcnt lgkmcnt(4)
	v_mfma_f32_16x16x32_bf16 v[140:143], v[72:75], v[144:147], v[140:143]
	v_mfma_f32_16x16x32_bf16 v[128:131], v[76:79], v[144:147], v[128:131]
	ds_read_b128 v[144:147], v168 offset:39168
	s_waitcnt lgkmcnt(4)
	v_mfma_f32_16x16x32_bf16 v[136:139], v[72:75], v[148:151], v[136:139]
	v_mfma_f32_16x16x32_bf16 v[132:135], v[76:79], v[148:151], v[132:135]
	ds_read_b128 v[148:151], v168 offset:40960
	s_waitcnt lgkmcnt(4)
	v_mfma_f32_16x16x32_bf16 v[140:143], v[80:83], v[156:159], v[140:143]
	v_mfma_f32_16x16x32_bf16 v[128:131], v[84:87], v[156:159], v[128:131]
	ds_read_b128 v[156:159], v168 offset:41216
	s_waitcnt lgkmcnt(4)
	v_mfma_f32_16x16x32_bf16 v[136:139], v[80:83], v[174:177], v[136:139]
	s_or_b32 s46, s9, 0x2000
	s_mov_b32 m0, s26
	s_nop 0
	buffer_load_dwordx4 v166, s[12:15], s46 offen lds
	v_mfma_f32_16x16x32_bf16 v[132:135], v[84:87], v[174:177], v[132:135]
	s_waitcnt lgkmcnt(3)
	v_mfma_f32_16x16x32_bf16 v[140:143], v[88:91], v[152:155], v[140:143]
	ds_read_b128 v[174:177], v168 offset:43008
	v_mfma_f32_16x16x32_bf16 v[128:131], v[92:95], v[152:155], v[128:131]
	ds_read_b128 v[152:155], v168 offset:43264
	s_waitcnt lgkmcnt(4)
	v_mfma_f32_16x16x32_bf16 v[136:139], v[88:91], v[144:147], v[136:139]
	v_mfma_f32_16x16x32_bf16 v[132:135], v[92:95], v[144:147], v[132:135]
	ds_read_b128 v[144:147], v168 offset:45056
	s_waitcnt lgkmcnt(4)
	v_mfma_f32_16x16x32_bf16 v[140:143], v[96:99], v[148:151], v[140:143]
	v_mfma_f32_16x16x32_bf16 v[128:131], v[100:103], v[148:151], v[128:131]
	ds_read_b128 v[148:151], v168 offset:45312
	s_waitcnt lgkmcnt(4)
	v_mfma_f32_16x16x32_bf16 v[136:139], v[96:99], v[156:159], v[136:139]
	s_or_b32 s46, s9, 0x8000
	s_mov_b32 m0, s27
	s_nop 0
	buffer_load_dwordx4 v166, s[12:15], s46 offen lds
	v_mfma_f32_16x16x32_bf16 v[132:135], v[100:103], v[156:159], v[132:135]
	s_waitcnt lgkmcnt(3)
	v_mfma_f32_16x16x32_bf16 v[140:143], v[104:107], v[174:177], v[140:143]
	ds_read_b128 v[178:181], v168 offset:47104
	v_mfma_f32_16x16x32_bf16 v[128:131], v[108:111], v[174:177], v[128:131]
	s_waitcnt lgkmcnt(3)
	v_mfma_f32_16x16x32_bf16 v[136:139], v[104:107], v[152:155], v[136:139]
	ds_read_b128 v[174:177], v168 offset:47360
	v_mfma_f32_16x16x32_bf16 v[132:135], v[108:111], v[152:155], v[132:135]
	ds_read_b128 v[156:159], v169
	s_waitcnt lgkmcnt(4)
	v_mfma_f32_16x16x32_bf16 v[140:143], v[112:115], v[144:147], v[140:143]
	v_mfma_f32_16x16x32_bf16 v[128:131], v[116:119], v[144:147], v[128:131]
	ds_read_b128 v[152:155], v170
	s_waitcnt lgkmcnt(4)
	v_mfma_f32_16x16x32_bf16 v[144:147], v[112:115], v[148:151], v[136:139]
	s_or_b32 s9, s9, 0xa000
	s_mov_b32 m0, s28
	s_nop 0
	buffer_load_dwordx4 v166, s[12:15], s9 offen lds
	v_mfma_f32_16x16x32_bf16 v[132:135], v[116:119], v[148:151], v[132:135]
	ds_read_b128 v[148:151], v171
	s_waitcnt lgkmcnt(4)
	v_mfma_f32_16x16x32_bf16 v[136:139], v[120:123], v[178:181], v[140:143]
	v_mfma_f32_16x16x32_bf16 v[128:131], v[124:127], v[178:181], v[128:131]
	s_waitcnt lgkmcnt(3)
	v_mfma_f32_16x16x32_bf16 v[140:143], v[120:123], v[174:177], v[144:147]
	s_nop 2
	ds_read_b128 v[144:147], v172
	v_mfma_f32_16x16x32_bf16 v[132:135], v[124:127], v[174:177], v[132:135]
	s_waitcnt vmcnt(4)
	s_barrier
	s_cmp_lg_u32 s8, s43
	s_cbranch_scc1 .LBB3_11
	s_and_saveexec_b64 s[8:9], s[0:1]
	s_cbranch_execnz .LBB3_38
	s_or_b64 exec, exec, s[8:9]
	s_and_saveexec_b64 s[8:9], s[2:3]
	s_cbranch_execnz .LBB3_39

.LBB3_9:
	s_mov_b32 s46, -1.0
	v_mov_b32_e32 v241, v135
	v_mov_b32_e32 v135, s46

.LBB3_22:
	v_mov_b32_e32 v241, v135
	v_mov_b32_e32 v135, s51

.LBB3_26:
	s_mov_b32 s78, 1
	v_mov_b32_e32 v240, v136
	v_mov_b32_e32 v136, s51
	s_or_b64 exec, exec, s[18:19]
	s_and_saveexec_b64 s[18:19], s[2:3]
	s_cbranch_execz .LBB3_16
.LBB3_27:
	v_mov_b32_e32 v240, v137
	v_mov_b32_e32 v137, s51
	s_or_b64 exec, exec, s[18:19]
	s_and_saveexec_b64 s[18:19], s[4:5]
	s_cbranch_execz .LBB3_17
.LBB3_28:
	v_mov_b32_e32 v240, v138
	v_mov_b32_e32 v138, s51
	s_or_b64 exec, exec, s[18:19]
	s_and_saveexec_b64 s[18:19], s[6:7]
	s_cbranch_execz .LBB3_18
.LBB3_29:
	v_mov_b32_e32 v240, v139
	v_mov_b32_e32 v139, s51
	s_or_b64 exec, exec, s[18:19]
	s_and_saveexec_b64 s[18:19], s[0:1]
	s_cbranch_execz .LBB3_19
.LBB3_30:
	v_mov_b32_e32 v241, v132
	v_mov_b32_e32 v132, s51
	s_or_b64 exec, exec, s[18:19]
	s_and_saveexec_b64 s[18:19], s[2:3]
	s_cbranch_execz .LBB3_20
.LBB3_31:
	v_mov_b32_e32 v241, v133
	v_mov_b32_e32 v133, s51
	s_or_b64 exec, exec, s[18:19]
	s_and_saveexec_b64 s[18:19], s[4:5]
	s_cbranch_execz .LBB3_21
.LBB3_32:
	v_mov_b32_e32 v241, v134
	v_mov_b32_e32 v134, s51
	s_or_b64 exec, exec, s[18:19]
	s_and_saveexec_b64 s[18:19], s[6:7]
	s_cbranch_execnz .LBB3_22
	s_branch .LBB3_23
.LBB3_33:
	s_waitcnt lgkmcnt(0)
	s_barrier
	s_add_i32 s60, s45, 16
	s_and_b32 s60, s60, 28
	s_or_b32 s60, s60, 2
	s_lshl_b32 s60, s60, 15
	s_or_b32 s61, s60, 0x4000
	s_mov_b32 m0, s38
	s_nop 0
	buffer_load_dwordx4 v166, s[12:15], s61 offen lds
	s_or_b32 s61, s60, 0x6000
	s_mov_b32 m0, s39
	s_nop 0
	buffer_load_dwordx4 v166, s[12:15], s61 offen lds
	s_or_b32 s61, s60, 0xc000
	s_mov_b32 m0, s40
	s_nop 0
	buffer_load_dwordx4 v166, s[12:15], s61 offen lds
	s_or_b32 s61, s60, 0xe000
	s_mov_b32 m0, s42
	s_nop 0
	buffer_load_dwordx4 v166, s[12:15], s61 offen lds
	s_lshr_b32 s62, s21, 1
	s_lshr_b32 s63, s20, 2
	s_xor_b32 s62, s62, s63
	s_and_b32 s62, s62, 1
	s_lshl_b32 s63, s62, 16
	v_add_u32_e32 v232, s63, v168
	v_add_u32_e32 v233, 0x8000, v232
	s_add_i32 s63, s45, 16
	s_and_b32 s63, s63, 28
	s_lshl_b32 s64, s62, 1
	s_or_b32 s63, s63, s64
	s_add_i32 s63, s63, s41
	s_lshl_b32 s63, s63, 1
	v_mov_b32_e32 v234, s63
	s_or_b32 s63, s63, 1
	v_mov_b32_e32 v235, s63
	s_lshl_b32 s64, s62, 8
	s_add_i32 s64, s64, s47
	s_add_i32 s64, s64, 0x20600
	v_lshl_add_u32 v236, v167, 2, s64
	s_waitcnt vmcnt(4)
	s_barrier
	s_movk_i32 s65, 0xffc0
	s_movk_i32 s66, 0xff80
	s_brev_b32 s67, -2
	s_add_i32 s68, s45, 12
	s_and_b32 s68, s68, 28
	s_or_b32 s68, s68, 2
	s_add_i32 s68, s68, s41
	s_lshl_b32 s68, s68, 1
	v_mov_b32_e32 v176, s68
	s_or_b32 s68, s68, 1
	v_mov_b32_e32 v177, s68
	s_add_i32 s68, s47, 0x20500
	v_lshl_add_u32 v182, v167, 2, s68
	ds_read_b128 v[144:147], v232 offset:0
	ds_read_b128 v[148:151], v232 offset:256
	ds_read_b128 v[152:155], v232 offset:2048
	ds_read_b128 v[156:159], v232 offset:2304
	ds_read_b128 v[224:227], v232 offset:4096
	s_waitcnt lgkmcnt(4)
	v_mfma_f32_16x16x32_bf16 v[208:211], v[0:3], v[144:147], 0
	v_mfma_f32_16x16x32_bf16 v[212:215], v[4:7], v[144:147], 0
	ds_read_b128 v[228:231], v232 offset:4352
	s_waitcnt lgkmcnt(4)
	v_mfma_f32_16x16x32_bf16 v[216:219], v[0:3], v[148:151], 0
	v_mfma_f32_16x16x32_bf16 v[220:223], v[4:7], v[148:151], 0
	ds_read_b128 v[144:147], v232 offset:6144
	s_waitcnt lgkmcnt(4)
	v_mfma_f32_16x16x32_bf16 v[208:211], v[8:11], v[152:155], v[208:211]
	v_mfma_f32_16x16x32_bf16 v[212:215], v[12:15], v[152:155], v[212:215]
	ds_read_b128 v[148:151], v232 offset:6400
	v_and_or_b32 v180, v136, s65, v176
	v_and_or_b32 v181, v140, s65, v177
	v_max3_f32 v161, v161, v180, v181
	v_and_b32_e32 v178, 0xffffff80, v136
	v_and_b32_e32 v179, 0xffffff80, v140
	s_waitcnt lgkmcnt(4)
	v_mfma_f32_16x16x32_bf16 v[216:219], v[8:11], v[156:159], v[216:219]
	v_mfma_f32_16x16x32_bf16 v[220:223], v[12:15], v[156:159], v[220:223]
	ds_read_b128 v[152:155], v232 offset:8192
	v_and_or_b32 v180, v137, s65, v176
	v_and_or_b32 v181, v141, s65, v177
	v_max3_f32 v160, v160, v180, v181
	v_and_or_b32 v180, v137, s66, 1
	v_and_or_b32 v181, v141, s66, 1
	v_max_f32_e32 v178, v178, v180
	v_max_f32_e32 v179, v179, v181
	s_waitcnt lgkmcnt(4)
	v_mfma_f32_16x16x32_bf16 v[208:211], v[16:19], v[224:227], v[208:211]
	v_mfma_f32_16x16x32_bf16 v[212:215], v[20:23], v[224:227], v[212:215]
	ds_read_b128 v[156:159], v232 offset:8448
	v_and_or_b32 v180, v138, s65, v176
	v_and_or_b32 v181, v142, s65, v177
	v_max3_f32 v162, v162, v180, v181
	v_and_or_b32 v180, v138, s66, 2
	v_and_or_b32 v181, v142, s66, 2
	v_max_f32_e32 v178, v178, v180
	v_max_f32_e32 v179, v179, v181
	s_waitcnt lgkmcnt(4)
	v_mfma_f32_16x16x32_bf16 v[216:219], v[16:19], v[228:231], v[216:219]
	v_mfma_f32_16x16x32_bf16 v[220:223], v[20:23], v[228:231], v[220:223]
	ds_read_b128 v[224:227], v232 offset:10240
	v_and_or_b32 v180, v139, s65, v176
	v_and_or_b32 v181, v143, s65, v177
	v_max3_f32 v163, v163, v180, v181
	v_and_or_b32 v180, v139, s66, 3
	v_and_or_b32 v181, v143, s66, 3
	v_max_f32_e32 v178, v178, v180
	v_max_f32_e32 v179, v179, v181
	s_waitcnt lgkmcnt(4)
	v_mfma_f32_16x16x32_bf16 v[208:211], v[24:27], v[144:147], v[208:211]
	v_mfma_f32_16x16x32_bf16 v[212:215], v[28:31], v[144:147], v[212:215]
	ds_read_b128 v[228:231], v232 offset:10496
	v_and_or_b32 v180, v128, s65, v176
	v_and_or_b32 v181, v132, s65, v177
	v_max3_f32 v203, v203, v180, v181
	v_and_or_b32 v180, v128, s66, 4
	v_and_or_b32 v181, v132, s66, 4
	v_max_f32_e32 v178, v178, v180
	v_max_f32_e32 v179, v179, v181
	s_waitcnt lgkmcnt(4)
	v_mfma_f32_16x16x32_bf16 v[216:219], v[24:27], v[148:151], v[216:219]
	v_mfma_f32_16x16x32_bf16 v[220:223], v[28:31], v[148:151], v[220:223]
	ds_read_b128 v[144:147], v232 offset:12288
	v_and_or_b32 v180, v129, s65, v176
	v_and_or_b32 v181, v133, s65, v177
	v_max3_f32 v204, v204, v180, v181
	v_and_or_b32 v180, v129, s66, 5
	v_and_or_b32 v181, v133, s66, 5
	v_max_f32_e32 v178, v178, v180
	v_max_f32_e32 v179, v179, v181
	s_waitcnt lgkmcnt(4)
	v_mfma_f32_16x16x32_bf16 v[208:211], v[32:35], v[152:155], v[208:211]
	v_mfma_f32_16x16x32_bf16 v[212:215], v[36:39], v[152:155], v[212:215]
	ds_read_b128 v[148:151], v232 offset:12544
	v_and_or_b32 v180, v130, s65, v176
	v_and_or_b32 v181, v134, s65, v177
	v_max3_f32 v205, v205, v180, v181
	v_and_or_b32 v180, v130, s66, 6
	v_and_or_b32 v181, v134, s66, 6
	v_max_f32_e32 v178, v178, v180
	v_max_f32_e32 v179, v179, v181
	s_waitcnt lgkmcnt(4)
	v_mfma_f32_16x16x32_bf16 v[216:219], v[32:35], v[156:159], v[216:219]
	v_mfma_f32_16x16x32_bf16 v[220:223], v[36:39], v[156:159], v[220:223]
	ds_read_b128 v[152:155], v232 offset:14336
	v_and_or_b32 v180, v131, s65, v176
	v_and_or_b32 v181, v135, s65, v177
	v_max3_f32 v206, v206, v180, v181
	v_and_or_b32 v180, v131, s66, 7
	v_and_or_b32 v181, v135, s66, 7
	v_max_f32_e32 v178, v178, v180
	v_max_f32_e32 v179, v179, v181
	s_waitcnt lgkmcnt(4)
	v_mfma_f32_16x16x32_bf16 v[208:211], v[40:43], v[224:227], v[208:211]
	v_mfma_f32_16x16x32_bf16 v[212:215], v[44:47], v[224:227], v[212:215]
	ds_read_b128 v[156:159], v232 offset:14592
	v_or_b32_e32 v183, v173, v178
	v_ashrrev_i32_e32 v180, 31, v178
	v_bitop3_b32 v183, v180, v183, s67 bitop3:0x6c
	v_or_b32_e32 v184, v173, v179
	v_ashrrev_i32_e32 v181, 31, v179
	v_bitop3_b32 v184, v181, v184, s67 bitop3:0x6c
	s_waitcnt lgkmcnt(4)
	v_mfma_f32_16x16x32_bf16 v[216:219], v[40:43], v[228:231], v[216:219]
	v_mfma_f32_16x16x32_bf16 v[220:223], v[44:47], v[228:231], v[220:223]
	s_waitcnt lgkmcnt(3)
	v_mfma_f32_16x16x32_bf16 v[208:211], v[48:51], v[144:147], v[208:211]
	v_mfma_f32_16x16x32_bf16 v[212:215], v[52:55], v[144:147], v[212:215]
	s_waitcnt lgkmcnt(2)
	v_mfma_f32_16x16x32_bf16 v[216:219], v[48:51], v[148:151], v[216:219]
	v_mfma_f32_16x16x32_bf16 v[220:223], v[52:55], v[148:151], v[220:223]
	s_waitcnt lgkmcnt(1)
	v_mfma_f32_16x16x32_bf16 v[208:211], v[56:59], v[152:155], v[208:211]
	v_mfma_f32_16x16x32_bf16 v[212:215], v[60:63], v[152:155], v[212:215]
	s_waitcnt lgkmcnt(0)
	v_mfma_f32_16x16x32_bf16 v[216:219], v[56:59], v[156:159], v[216:219]
	v_mfma_f32_16x16x32_bf16 v[220:223], v[60:63], v[156:159], v[220:223]
	s_waitcnt vmcnt(0)
	s_barrier
	ds_read_b128 v[144:147], v233 offset:0
	ds_read_b128 v[148:151], v233 offset:256
	ds_read_b128 v[152:155], v233 offset:2048
	ds_read_b128 v[156:159], v233 offset:2304
	ds_read_b128 v[224:227], v233 offset:4096
	s_waitcnt lgkmcnt(4)
	v_mfma_f32_16x16x32_bf16 v[208:211], v[64:67], v[144:147], v[208:211]
	v_mfma_f32_16x16x32_bf16 v[212:215], v[68:71], v[144:147], v[212:215]
	ds_read_b128 v[228:231], v233 offset:4352
	s_waitcnt lgkmcnt(4)
	v_mfma_f32_16x16x32_bf16 v[216:219], v[64:67], v[148:151], v[216:219]
	v_mfma_f32_16x16x32_bf16 v[220:223], v[68:71], v[148:151], v[220:223]
	ds_read_b128 v[144:147], v233 offset:6144
	s_waitcnt lgkmcnt(4)
	v_mfma_f32_16x16x32_bf16 v[208:211], v[72:75], v[152:155], v[208:211]
	v_mfma_f32_16x16x32_bf16 v[212:215], v[76:79], v[152:155], v[212:215]
	ds_read_b128 v[148:151], v233 offset:6400
	s_waitcnt lgkmcnt(4)
	v_mfma_f32_16x16x32_bf16 v[216:219], v[72:75], v[156:159], v[216:219]
	v_mfma_f32_16x16x32_bf16 v[220:223], v[76:79], v[156:159], v[220:223]
	ds_read_b128 v[152:155], v233 offset:8192
	s_waitcnt lgkmcnt(4)
	v_mfma_f32_16x16x32_bf16 v[208:211], v[80:83], v[224:227], v[208:211]
	v_mfma_f32_16x16x32_bf16 v[212:215], v[84:87], v[224:227], v[212:215]
	ds_read_b128 v[156:159], v233 offset:8448
	s_waitcnt lgkmcnt(4)
	v_mfma_f32_16x16x32_bf16 v[216:219], v[80:83], v[228:231], v[216:219]
	v_mfma_f32_16x16x32_bf16 v[220:223], v[84:87], v[228:231], v[220:223]
	ds_read_b128 v[224:227], v233 offset:10240
	s_waitcnt lgkmcnt(4)
	v_mfma_f32_16x16x32_bf16 v[208:211], v[88:91], v[144:147], v[208:211]
	v_mfma_f32_16x16x32_bf16 v[212:215], v[92:95], v[144:147], v[212:215]
	ds_read_b128 v[228:231], v233 offset:10496
	s_waitcnt lgkmcnt(4)
	v_mfma_f32_16x16x32_bf16 v[216:219], v[88:91], v[148:151], v[216:219]
	v_mfma_f32_16x16x32_bf16 v[220:223], v[92:95], v[148:151], v[220:223]
	ds_read_b128 v[144:147], v233 offset:12288
	s_waitcnt lgkmcnt(4)
	v_mfma_f32_16x16x32_bf16 v[208:211], v[96:99], v[152:155], v[208:211]
	v_mfma_f32_16x16x32_bf16 v[212:215], v[100:103], v[152:155], v[212:215]
	ds_read_b128 v[148:151], v233 offset:12544
	s_waitcnt lgkmcnt(4)
	v_mfma_f32_16x16x32_bf16 v[216:219], v[96:99], v[156:159], v[216:219]
	v_mfma_f32_16x16x32_bf16 v[220:223], v[100:103], v[156:159], v[220:223]
	ds_read_b128 v[152:155], v233 offset:14336
	s_waitcnt lgkmcnt(4)
	v_mfma_f32_16x16x32_bf16 v[208:211], v[104:107], v[224:227], v[208:211]
	v_mfma_f32_16x16x32_bf16 v[212:215], v[108:111], v[224:227], v[212:215]
	ds_read_b128 v[156:159], v233 offset:14592
	s_waitcnt lgkmcnt(4)
	v_mfma_f32_16x16x32_bf16 v[216:219], v[104:107], v[228:231], v[216:219]
	v_mfma_f32_16x16x32_bf16 v[220:223], v[108:111], v[228:231], v[220:223]
	s_waitcnt lgkmcnt(3)
	v_mfma_f32_16x16x32_bf16 v[208:211], v[112:115], v[144:147], v[208:211]
	v_mfma_f32_16x16x32_bf16 v[212:215], v[116:119], v[144:147], v[212:215]
	s_waitcnt lgkmcnt(2)
	v_mfma_f32_16x16x32_bf16 v[216:219], v[112:115], v[148:151], v[216:219]
	v_mfma_f32_16x16x32_bf16 v[220:223], v[116:119], v[148:151], v[220:223]
	s_waitcnt lgkmcnt(1)
	v_mfma_f32_16x16x32_bf16 v[208:211], v[120:123], v[152:155], v[208:211]
	v_mfma_f32_16x16x32_bf16 v[212:215], v[124:127], v[152:155], v[212:215]
	s_waitcnt lgkmcnt(0)
	v_mfma_f32_16x16x32_bf16 v[216:219], v[120:123], v[156:159], v[216:219]
	v_mfma_f32_16x16x32_bf16 v[220:223], v[124:127], v[156:159], v[220:223]
	s_nop 7
	s_nop 3
	v_and_or_b32 v237, v208, s65, v234
	v_and_or_b32 v238, v216, s65, v235
	v_max3_f32 v161, v161, v237, v238
	v_and_b32_e32 v174, 0xffffff80, v208
	v_and_b32_e32 v175, 0xffffff80, v216
	v_and_or_b32 v237, v209, s65, v234
	v_and_or_b32 v238, v217, s65, v235
	v_max3_f32 v160, v160, v237, v238
	v_and_or_b32 v237, v209, s66, 1
	v_and_or_b32 v238, v217, s66, 1
	v_max_f32_e32 v174, v174, v237
	v_max_f32_e32 v175, v175, v238
	v_and_or_b32 v237, v210, s65, v234
	v_and_or_b32 v238, v218, s65, v235
	v_max3_f32 v162, v162, v237, v238
	v_and_or_b32 v237, v210, s66, 2
	v_and_or_b32 v238, v218, s66, 2
	v_max_f32_e32 v174, v174, v237
	v_max_f32_e32 v175, v175, v238
	v_and_or_b32 v237, v211, s65, v234
	v_and_or_b32 v238, v219, s65, v235
	v_max3_f32 v163, v163, v237, v238
	v_and_or_b32 v237, v211, s66, 3
	v_and_or_b32 v238, v219, s66, 3
	v_max_f32_e32 v174, v174, v237
	v_max_f32_e32 v175, v175, v238
	v_and_or_b32 v237, v212, s65, v234
	v_and_or_b32 v238, v220, s65, v235
	v_max3_f32 v203, v203, v237, v238
	v_and_or_b32 v237, v212, s66, 4
	v_and_or_b32 v238, v220, s66, 4
	v_max_f32_e32 v174, v174, v237
	v_max_f32_e32 v175, v175, v238
	v_and_or_b32 v237, v213, s65, v234
	v_and_or_b32 v238, v221, s65, v235
	v_max3_f32 v204, v204, v237, v238
	v_and_or_b32 v237, v213, s66, 5
	v_and_or_b32 v238, v221, s66, 5
	v_max_f32_e32 v174, v174, v237
	v_max_f32_e32 v175, v175, v238
	v_and_or_b32 v237, v214, s65, v234
	v_and_or_b32 v238, v222, s65, v235
	v_max3_f32 v205, v205, v237, v238
	v_and_or_b32 v237, v214, s66, 6
	v_and_or_b32 v238, v222, s66, 6
	v_max_f32_e32 v174, v174, v237
	v_max_f32_e32 v175, v175, v238
	v_and_or_b32 v237, v215, s65, v234
	v_and_or_b32 v238, v223, s65, v235
	v_max3_f32 v206, v206, v237, v238
	v_and_or_b32 v237, v215, s66, 7
	v_and_or_b32 v238, v223, s66, 7
	v_max_f32_e32 v174, v174, v237
	v_max_f32_e32 v175, v175, v238
	v_or_b32_e32 v237, v173, v174
	v_ashrrev_i32_e32 v238, 31, v174
	v_bitop3_b32 v237, v238, v237, s67 bitop3:0x6c
	ds_max_i32 v236, v237
	v_or_b32_e32 v237, v173, v175
	v_ashrrev_i32_e32 v238, 31, v175
	v_bitop3_b32 v237, v238, v237, s67 bitop3:0x6c
	ds_max_i32 v236, v237 offset:64
	ds_max_i32 v182, v183
	ds_max_i32 v182, v184 offset:64
	v_mov_b32_e32 v0, v161
	v_mov_b32_e32 v1, v160
	v_mov_b32_e32 v3, v162
	v_mov_b32_e32 v4, v163
	v_mov_b32_e32 v5, v203
	v_mov_b32_e32 v6, v204
	v_mov_b32_e32 v7, v205
	v_mov_b32_e32 v8, v206
	s_cmp_lg_u32 s78, 1
	s_cbranch_scc1 .Lsq_done
	s_or_b64 s[70:71], s[0:1], s[2:3]
	s_or_b64 s[72:73], s[4:5], s[6:7]
	s_or_b64 s[70:71], s[70:71], s[72:73]
	s_mov_b64 s[72:73], exec
	s_mov_b64 exec, s[70:71]
	global_store_dword v[164:165], v240, off
	global_store_dword v[164:165], v241, off offset:64
	s_mov_b64 exec, s[72:73]
.Lsq_done:
	s_movk_i32 s2, 0xff80
	s_brev_b32 s3, -2
	v_mbcnt_lo_u32_b32 v2, -1, 0
	s_andn2_b32 s23, s23, 63
	s_lshl_b64 s[0:1], s[16:17], 13
	v_mbcnt_hi_u32_b32 v2, -1, v2
	s_add_u32 s4, s10, s0
	v_add_u32_e32 v9, s23, v2
	s_addc_u32 s5, s11, s1
	s_mov_b32 s6, 4
	s_lshl_b32 s0, s6, 7
	v_cmp_gt_i32_e32 vcc, s0, v9
	s_waitcnt lgkmcnt(0)
	s_barrier
	s_and_saveexec_b64 s[0:1], vcc
	s_cbranch_execz .LBB3_35
	v_mov_b32_e32 v10, 0x20000
	v_lshl_add_u32 v10, v9, 2, v10
	ds_read_b32 v10, v10
	s_movk_i32 s6, 0x63
	v_and_b32_e32 v12, 0x7f, v9
	s_waitcnt lgkmcnt(0)
	v_ashrrev_i32_e32 v11, 31, v10
	v_and_b32_e32 v13, 0x7fffffff, v11
	v_bitop3_b32 v11, v11, v10, s3 bitop3:0x6c
	v_lshlrev_b32_e32 v14, 2, v11
	v_and_b32_e32 v14, 16, v14
	s_lshl_b32 s3, s20, 7
	v_bitop3_b32 v13, v13, s6, v10 bitop3:0x48
	v_or3_b32 v13, v13, s3, v14
	v_bfrev_b32_e32 v14, 1
	v_cmp_lt_i32_e32 vcc, -1, v10
	v_lshrrev_b32_e32 v15, 1, v11
	v_and_b32_e32 v15, 12, v15
	v_cndmask_b32_e32 v10, -1, v14, vcc
	v_bitop3_b32 v11, v11, v10, s2 bitop3:0x6c
	s_movk_i32 s2, 0x3ff
	v_bitop3_b32 v10, v13, s2, v15 bitop3:0x36
	s_lshl_b32 s2, s22, 7
	s_addk_i32 s2, 0x80
	v_add_u32_e32 v9, s2, v9
	s_movk_i32 s2, 0x380
	v_and_or_b32 v9, v9, s2, v12
	v_lshlrev_b32_e32 v9, 3, v9
	global_atomic_umax_x2 v9, v[10:11], s[4:5]

.LBB3_38:
	s_mov_b32 s78, 1
	s_mov_b32 s46, -1.0
	v_mov_b32_e32 v240, v136
	v_mov_b32_e32 v136, s46
	s_or_b64 exec, exec, s[8:9]
	s_and_saveexec_b64 s[8:9], s[2:3]
	s_cbranch_execz .LBB3_3
.LBB3_39:
	s_mov_b32 s46, -1.0
	v_mov_b32_e32 v240, v137
	v_mov_b32_e32 v137, s46
	s_or_b64 exec, exec, s[8:9]
	s_and_saveexec_b64 s[8:9], s[4:5]
	s_cbranch_execz .LBB3_4
.LBB3_40:
	s_mov_b32 s46, -1.0
	v_mov_b32_e32 v240, v138
	v_mov_b32_e32 v138, s46
	s_or_b64 exec, exec, s[8:9]
	s_and_saveexec_b64 s[8:9], s[6:7]
	s_cbranch_execz .LBB3_5
.LBB3_41:
	s_mov_b32 s46, -1.0
	v_mov_b32_e32 v240, v139
	v_mov_b32_e32 v139, s46
	s_or_b64 exec, exec, s[8:9]
	s_and_saveexec_b64 s[8:9], s[0:1]
	s_cbranch_execz .LBB3_6
.LBB3_42:
	s_mov_b32 s46, -1.0
	v_mov_b32_e32 v241, v132
	v_mov_b32_e32 v132, s46
	s_or_b64 exec, exec, s[8:9]
	s_and_saveexec_b64 s[8:9], s[2:3]
	s_cbranch_execz .LBB3_7
.LBB3_43:
	s_mov_b32 s46, -1.0
	v_mov_b32_e32 v241, v133
	v_mov_b32_e32 v133, s46
	s_or_b64 exec, exec, s[8:9]
	s_and_saveexec_b64 s[8:9], s[4:5]
	s_cbranch_execz .LBB3_8
.LBB3_44:
	s_mov_b32 s46, -1.0
	v_mov_b32_e32 v241, v134
	v_mov_b32_e32 v134, s46
	s_or_b64 exec, exec, s[8:9]
	s_and_saveexec_b64 s[8:9], s[6:7]
	s_cbranch_execnz .LBB3_9
	s_branch .LBB3_10

	.amdhsa_kernel _Z6k_gramILi0EEvPK15HIP_vector_typeIjLj4EEPyPf
		.amdhsa_group_segment_fixed_size 133120
		.amdhsa_private_segment_fixed_size 0
		.amdhsa_kernarg_size 24
		.amdhsa_user_sgpr_count 2
		.amdhsa_user_sgpr_dispatch_ptr 0
		.amdhsa_user_sgpr_queue_ptr 0
		.amdhsa_user_sgpr_kernarg_segment_ptr 1
		.amdhsa_user_sgpr_dispatch_id 0
		.amdhsa_user_sgpr_kernarg_preload_length 0
		.amdhsa_user_sgpr_kernarg_preload_offset 0
		.amdhsa_user_sgpr_private_segment_size 0
		.amdhsa_uses_dynamic_stack 0
		.amdhsa_enable_private_segment 0
		.amdhsa_system_sgpr_workgroup_id_x 1
		.amdhsa_system_sgpr_workgroup_id_y 0
		.amdhsa_system_sgpr_workgroup_id_z 0
		.amdhsa_system_sgpr_workgroup_info 0
		.amdhsa_system_vgpr_workitem_id 0
		.amdhsa_next_free_vgpr 242
		.amdhsa_next_free_sgpr 96
		.amdhsa_accum_offset 244
		.amdhsa_reserve_vcc 1
		.amdhsa_float_round_mode_32 0
		.amdhsa_float_round_mode_16_64 0
		.amdhsa_float_denorm_mode_32 3
		.amdhsa_float_denorm_mode_16_64 3
		.amdhsa_dx10_clamp 1
		.amdhsa_ieee_mode 1
		.amdhsa_fp16_overflow 0
		.amdhsa_tg_split 0
		.amdhsa_exception_fp_ieee_invalid_op 0
		.amdhsa_exception_fp_denorm_src 0
		.amdhsa_exception_fp_ieee_div_zero 0
		.amdhsa_exception_fp_ieee_overflow 0
		.amdhsa_exception_fp_ieee_underflow 0
		.amdhsa_exception_fp_ieee_inexact 0
		.amdhsa_exception_int_div_zero 0
	.end_amdhsa_kernel

amdhsa.kernels:
  - .agpr_count:     0
    .args:
      - .actual_access:  read_only
        .address_space:  global
        .offset:         0
        .size:           8
        .value_kind:     global_buffer
      - .actual_access:  write_only
        .address_space:  global
        .offset:         8
        .size:           8
        .value_kind:     global_buffer
      - .actual_access:  write_only
        .address_space:  global
        .offset:         16
        .size:           8
        .value_kind:     global_buffer
      - .actual_access:  write_only
        .address_space:  global
        .offset:         24
        .size:           8
        .value_kind:     global_buffer
      - .actual_access:  write_only
        .address_space:  global
        .offset:         32
        .size:           8
        .value_kind:     global_buffer
    .group_segment_fixed_size: 32768
    .kernarg_segment_align: 8
    .kernarg_segment_size: 40
    .language:       OpenCL C
    .language_version:
      - 2
      - 0
    .max_flat_workgroup_size: 256
    .name:           _Z6k_normPKfP15HIP_vector_typeIjLj4EEPfPyS4_
    .private_segment_fixed_size: 0
    .sgpr_count:     16
    .sgpr_spill_count: 0
    .symbol:         _Z6k_normPKfP15HIP_vector_typeIjLj4EEPfPyS4_.kd
    .uniform_work_group_size: 1
    .uses_dynamic_stack: false
    .vgpr_count:     90
    .vgpr_spill_count: 0
    .wavefront_size: 64
  - .agpr_count:     0
    .args:
      - .actual_access:  read_only
        .address_space:  global
        .offset:         0
        .size:           8
        .value_kind:     global_buffer
      - .actual_access:  read_only
        .address_space:  global
        .offset:         8
        .size:           8
        .value_kind:     global_buffer
      - .actual_access:  read_only
        .address_space:  global
        .offset:         16
        .size:           8
        .value_kind:     global_buffer
      - .actual_access:  read_only
        .address_space:  global
        .offset:         24
        .size:           8
        .value_kind:     global_buffer
      - .address_space:  global
        .offset:         32
        .size:           8
        .value_kind:     global_buffer
    .group_segment_fixed_size: 64
    .kernarg_segment_align: 8
    .kernarg_segment_size: 40
    .language:       OpenCL C
    .language_version:
      - 2
      - 0
    .max_flat_workgroup_size: 1024
    .name:           _Z6k_distPKyPKfS2_PK15HIP_vector_typeIjLj4EEPf
    .private_segment_fixed_size: 0
    .sgpr_count:     16
    .sgpr_spill_count: 0
    .symbol:         _Z6k_distPKyPKfS2_PK15HIP_vector_typeIjLj4EEPf.kd
    .uniform_work_group_size: 1
    .uses_dynamic_stack: false
    .vgpr_count:     17
    .vgpr_spill_count: 0
    .wavefront_size: 64
  - .agpr_count:     0
    .args:
      - .actual_access:  read_only
        .address_space:  global
        .offset:         0
        .size:           8
        .value_kind:     global_buffer
      - .actual_access:  write_only
        .address_space:  global
        .offset:         8
        .size:           8
        .value_kind:     global_buffer
    .group_segment_fixed_size: 0
    .kernarg_segment_align: 8
    .kernarg_segment_size: 16
    .language:       OpenCL C
    .language_version:
      - 2
      - 0
    .max_flat_workgroup_size: 64
    .name:           _Z7k_finalPKfPf
    .private_segment_fixed_size: 0
    .sgpr_count:     12
    .sgpr_spill_count: 0
    .symbol:         _Z7k_finalPKfPf.kd
    .uniform_work_group_size: 1
    .uses_dynamic_stack: false
    .vgpr_count:     6
    .vgpr_spill_count: 0
    .wavefront_size: 64
  - .agpr_count:     0
    .args:
      - .address_space:  global
        .offset:         0
        .size:           8
        .value_kind:     global_buffer
      - .address_space:  global
        .offset:         8
        .size:           8
        .value_kind:     global_buffer
      - .actual_access:  write_only
        .address_space:  global
        .offset:         16
        .size:           8
        .value_kind:     global_buffer
    .group_segment_fixed_size: 133120
    .kernarg_segment_align: 8
    .kernarg_segment_size: 24
    .language:       OpenCL C
    .language_version:
      - 2
      - 0
    .max_flat_workgroup_size: 512
    .name:           _Z6k_gramILi0EEvPK15HIP_vector_typeIjLj4EEPyPf
    .private_segment_fixed_size: 0
    .sgpr_count:     64
    .sgpr_spill_count: 0
    .symbol:         _Z6k_gramILi0EEvPK15HIP_vector_typeIjLj4EEPyPf.kd
    .uniform_work_group_size: 1
    .uses_dynamic_stack: false
    .vgpr_count:     242
    .vgpr_spill_count: 0
    .wavefront_size: 64
